# gemm: balanced fragment-read split - ks1 fragments of the current tile are read under the ks0 MFMAs, ks0 fragments of the next tile under the ks1 MFMAs (9 reads + 3 DMAs per 18-MFMA block)
# speedup vs baseline: 1.0275x; 1.0124x over previous
_Z8gemm_qkvPKDF16_S0_PKfPDF16_S3_S3_Pj:
	v_readfirstlane_b32 s13, v0
	s_lshr_b32 s8, s13, 6
	v_bfe_u32 v2, v0, 3, 3
	s_load_dwordx4 s[4:7], s[0:1], 0x0
	v_lshl_or_b32 v6, s8, 3, v2
	v_lshrrev_b32_e32 v2, 1, v6
	s_mul_i32 s16, s3, 0xc0
	v_xor_b32_e32 v4, v2, v0
	v_add_u32_e32 v2, s16, v6
	v_ashrrev_i32_e32 v3, 31, v2
	s_bfe_u32 s15, s13, 0x20006
	v_lshlrev_b64 v[2:3], 11, v[2:3]
	v_lshlrev_b32_e32 v4, 4, v4
	s_mul_i32 s10, s2, 0xc0
	s_mul_i32 s2, s15, 48
	s_waitcnt lgkmcnt(0)
	v_lshl_add_u64 v[2:3], s[4:5], 0, v[2:3]
	v_and_b32_e32 v4, 0x70, v4
	v_mov_b32_e32 v5, 0
	s_add_i32 s17, s2, s10
	v_lshl_add_u64 v[218:219], v[2:3], 0, v[4:5]
	v_add_u32_e32 v2, s10, v6
	s_lshl_b32 s8, s8, 10
	v_ashrrev_i32_e32 v3, 31, v2
	s_cmp_lg_u32 0x400, -1
	v_lshlrev_b64 v[2:3], 11, v[2:3]
	s_cselect_b32 s4, 0x400, 0
	v_lshl_add_u64 v[2:3], s[6:7], 0, v[2:3]
	s_add_i32 s11, s8, s4
	s_mov_b32 s4, m0
	s_mov_b32 m0, s11
	s_nop 0
	global_load_lds_dwordx4 v[218:219], off
	s_mov_b32 m0, s4
	v_lshl_add_u64 v[220:221], v[2:3], 0, v[4:5]
	s_add_i32 s4, s11, 0x6000
	s_mov_b32 s5, m0
	s_mov_b32 m0, s4
	s_nop 0
	global_load_lds_dwordx4 v[220:221], off
	s_mov_b32 m0, s5
	s_mov_b64 s[4:5], 0x20000
	v_lshl_add_u64 v[222:223], v[218:219], 0, s[4:5]
	s_add_i32 s9, s11, 0x2000
	s_mov_b32 s6, m0
	s_mov_b32 m0, s9
	s_nop 0
	global_load_lds_dwordx4 v[222:223], off
	s_mov_b32 m0, s6
	v_lshl_add_u64 v[224:225], v[220:221], 0, s[4:5]
	s_add_i32 s4, s11, 0x8000
	s_mov_b32 s5, m0
	s_mov_b32 m0, s4
	s_nop 0
	global_load_lds_dwordx4 v[224:225], off
	s_mov_b32 m0, s5
	s_mov_b64 s[4:5], 0x40000
	v_lshl_add_u64 v[226:227], v[218:219], 0, s[4:5]
	s_add_i32 s12, s11, 0x4000
	s_mov_b32 s6, m0
	s_mov_b32 m0, s12
	s_nop 0
	global_load_lds_dwordx4 v[226:227], off
	s_mov_b32 m0, s6
	v_lshl_add_u64 v[228:229], v[220:221], 0, s[4:5]
	s_add_i32 s4, s11, 0xa000
	s_mov_b32 s5, m0
	s_mov_b32 m0, s4
	s_nop 0
	global_load_lds_dwordx4 v[228:229], off
	s_mov_b32 m0, s5
	s_cmpk_gt_i32 s17, 0x7d0
	s_cselect_b64 s[4:5], -1, 0
	s_lshr_b32 s14, s13, 8
	s_mul_i32 s6, s14, 0x3000
	s_add_i32 s13, s6, 0x400
	s_mov_b64 s[6:7], 0x80
	s_add_i32 s18, s11, 0xc000
	v_lshl_add_u64 v[2:3], v[218:219], 0, s[6:7]
	s_mov_b32 s30, m0
	s_mov_b32 m0, s18
	s_nop 0
	global_load_lds_dwordx4 v[2:3], off
	s_mov_b32 m0, s30
	s_add_i32 s19, s11, 0x12000
	v_lshl_add_u64 v[2:3], v[220:221], 0, s[6:7]
	s_mov_b32 s6, m0
	s_mov_b32 m0, s19
	s_nop 0
	global_load_lds_dwordx4 v[2:3], off
	s_mov_b32 m0, s6
	s_mov_b64 s[6:7], 0x20080
	s_add_i32 s20, s11, 0xe000
	v_lshl_add_u64 v[2:3], v[218:219], 0, s[6:7]
	s_mov_b32 s18, m0
	s_mov_b32 m0, s20
	s_nop 0
	global_load_lds_dwordx4 v[2:3], off
	s_mov_b32 m0, s18
	s_add_i32 s21, s11, 0x14000
	v_lshl_add_u64 v[2:3], v[220:221], 0, s[6:7]
	s_mov_b32 s6, m0
	s_mov_b32 m0, s21
	s_nop 0
	global_load_lds_dwordx4 v[2:3], off
	s_mov_b32 m0, s6
	s_mov_b64 s[6:7], 0x40080
	v_lshl_add_u64 v[2:3], v[218:219], 0, s[6:7]
	s_add_i32 s22, s11, 0x10000
	s_mov_b32 s18, m0
	s_mov_b32 m0, s22
	s_nop 0
	global_load_lds_dwordx4 v[2:3], off
	s_mov_b32 m0, s18
	v_lshl_add_u64 v[2:3], v[220:221], 0, s[6:7]
	v_and_b32_e32 v1, 15, v0
	v_bfe_u32 v231, v0, 4, 2
	s_add_i32 s23, s11, 0x16000
	s_mov_b32 s6, m0
	s_mov_b32 m0, s23
	s_nop 0
	global_load_lds_dwordx4 v[2:3], off
	s_mov_b32 m0, s6
	v_lshrrev_b32_e32 v3, 1, v0
	v_lshlrev_b32_e32 v2, 7, v1
	v_bfe_u32 v4, v0, 1, 3
	v_bitop3_b32 v3, v231, v3, 7 bitop3:0x78
	v_lshl_or_b32 v238, v3, 4, v2
	v_bitop3_b32 v3, v231, v4, 4 bitop3:0x36
	v_lshl_or_b32 v240, v3, 4, v2
	s_mulk_i32 s15, 0x1800
	s_addk_i32 s15, 0x6400
	v_add_u32_e32 v158, s13, v238
	v_add_u32_e32 v160, s13, v240
	v_add_u32_e32 v162, s15, v238
	v_add_u32_e32 v164, s15, v240
	s_add_u32 m0, s11, 0x17f00
	s_nop 0
	global_load_lds_dwordx4 v[218:219], off offset:256
	s_add_u32 m0, s11, 0x19f00
	s_nop 0
	global_load_lds_dwordx4 v[222:223], off offset:256
	s_add_u32 m0, s11, 0x1bf00
	s_nop 0
	global_load_lds_dwordx4 v[226:227], off offset:256
	s_load_dwordx2 s[24:25], s[0:1], 0x10
	s_mov_b32 s20, 0x180
	s_mov_b32 s21, 0
	v_lshl_add_u64 v[218:219], v[218:219], 0, s[20:21]
	v_lshl_add_u64 v[222:223], v[222:223], 0, s[20:21]
	v_lshl_add_u64 v[226:227], v[226:227], 0, s[20:21]
	v_lshl_add_u64 v[220:221], v[220:221], 0, s[20:21]
	v_lshl_add_u64 v[224:225], v[224:225], 0, s[20:21]
	v_lshl_add_u64 v[228:229], v[228:229], 0, s[20:21]
	v_add_u32_e32 v159, 0x18000, v158
	v_add_u32_e32 v161, 0x18000, v160
	v_add_u32_e32 v163, 0x18000, v162
	v_add_u32_e32 v165, 0x18000, v164
	v_mov_b32_e32 v82, 0
	v_mov_b32_e32 v83, 0
	v_mov_b32_e32 v84, 0
	v_mov_b32_e32 v85, 0
	v_mov_b32_e32 v58, 0
	v_mov_b32_e32 v59, 0
	v_mov_b32_e32 v60, 0
	v_mov_b32_e32 v61, 0
	v_mov_b32_e32 v14, 0
	v_mov_b32_e32 v15, 0
	v_mov_b32_e32 v16, 0
	v_mov_b32_e32 v17, 0
	v_mov_b32_e32 v78, 0
	v_mov_b32_e32 v79, 0
	v_mov_b32_e32 v80, 0
	v_mov_b32_e32 v81, 0
	v_mov_b32_e32 v22, 0
	v_mov_b32_e32 v23, 0
	v_mov_b32_e32 v24, 0
	v_mov_b32_e32 v25, 0
	v_mov_b32_e32 v30, 0
	v_mov_b32_e32 v31, 0
	v_mov_b32_e32 v32, 0
	v_mov_b32_e32 v33, 0
	v_mov_b32_e32 v74, 0
	v_mov_b32_e32 v75, 0
	v_mov_b32_e32 v76, 0
	v_mov_b32_e32 v77, 0
	v_mov_b32_e32 v18, 0
	v_mov_b32_e32 v19, 0
	v_mov_b32_e32 v20, 0
	v_mov_b32_e32 v21, 0
	v_mov_b32_e32 v26, 0
	v_mov_b32_e32 v27, 0
	v_mov_b32_e32 v28, 0
	v_mov_b32_e32 v29, 0
	v_mov_b32_e32 v70, 0
	v_mov_b32_e32 v71, 0
	v_mov_b32_e32 v72, 0
	v_mov_b32_e32 v73, 0
	v_mov_b32_e32 v46, 0
	v_mov_b32_e32 v47, 0
	v_mov_b32_e32 v48, 0
	v_mov_b32_e32 v49, 0
	v_mov_b32_e32 v240, 0
	v_mov_b32_e32 v241, 0
	v_mov_b32_e32 v242, 0
	v_mov_b32_e32 v243, 0
	v_mov_b32_e32 v66, 0
	v_mov_b32_e32 v67, 0
	v_mov_b32_e32 v68, 0
	v_mov_b32_e32 v69, 0
	v_mov_b32_e32 v42, 0
	v_mov_b32_e32 v43, 0
	v_mov_b32_e32 v44, 0
	v_mov_b32_e32 v45, 0
	v_mov_b32_e32 v236, 0
	v_mov_b32_e32 v237, 0
	v_mov_b32_e32 v238, 0
	v_mov_b32_e32 v239, 0
	v_mov_b32_e32 v62, 0
	v_mov_b32_e32 v63, 0
	v_mov_b32_e32 v64, 0
	v_mov_b32_e32 v65, 0
	v_mov_b32_e32 v38, 0
	v_mov_b32_e32 v39, 0
	v_mov_b32_e32 v40, 0
	v_mov_b32_e32 v41, 0
	v_mov_b32_e32 v34, 0
	v_mov_b32_e32 v35, 0
	v_mov_b32_e32 v36, 0
	v_mov_b32_e32 v37, 0
	s_not_b64 s[6:7], s[4:5]
	s_mov_b32 s22, 4
	s_waitcnt vmcnt(9) lgkmcnt(0)
	s_barrier
	ds_read_b128 v[134:137], v162
	ds_read_b128 v[138:141], v162 offset:2048
	ds_read_b128 v[142:145], v162 offset:4096
	ds_read_b128 v[86:89], v158
	ds_read_b128 v[90:93], v158 offset:2048
	ds_read_b128 v[94:97], v158 offset:4096
	ds_read_b128 v[98:101], v158 offset:6144
	ds_read_b128 v[102:105], v158 offset:8192
	ds_read_b128 v[106:109], v158 offset:10240
	s_and_b64 vcc, exec, s[4:5]
	s_cbranch_vccnz .Lgemm_N_loop
.Lgemm_T_loop:
	s_waitcnt lgkmcnt(0)
	s_add_u32 m0, s11, 0x1e080
	ds_read_b128 v[146:149], v164
	global_load_lds_dwordx4 v[220:221], off offset:-128
	v_mfma_f32_16x16x32_f16 v[82:85], v[134:137], v[86:89], v[82:85]
	ds_read_b128 v[150:153], v164 offset:2048
	v_mfma_f32_16x16x32_f16 v[58:61], v[138:141], v[86:89], v[58:61]
	ds_read_b128 v[154:157], v164 offset:4096
	v_mfma_f32_16x16x32_f16 v[14:17], v[142:145], v[86:89], v[14:17]
	ds_read_b128 v[110:113], v160
	v_mfma_f32_16x16x32_f16 v[78:81], v[134:137], v[90:93], v[78:81]
	ds_read_b128 v[114:117], v160 offset:2048
	v_mfma_f32_16x16x32_f16 v[22:25], v[138:141], v[90:93], v[22:25]
	ds_read_b128 v[118:121], v160 offset:4096
	v_mfma_f32_16x16x32_f16 v[30:33], v[142:145], v[90:93], v[30:33]
	s_add_u32 m0, s11, 0x20080
	ds_read_b128 v[122:125], v160 offset:6144
	global_load_lds_dwordx4 v[224:225], off offset:-128
	v_mfma_f32_16x16x32_f16 v[74:77], v[134:137], v[94:97], v[74:77]
	ds_read_b128 v[126:129], v160 offset:8192
	v_mfma_f32_16x16x32_f16 v[18:21], v[138:141], v[94:97], v[18:21]
	ds_read_b128 v[130:133], v160 offset:10240
	v_mfma_f32_16x16x32_f16 v[26:29], v[142:145], v[94:97], v[26:29]
	v_mfma_f32_16x16x32_f16 v[70:73], v[134:137], v[98:101], v[70:73]
	v_mfma_f32_16x16x32_f16 v[46:49], v[138:141], v[98:101], v[46:49]
	v_mfma_f32_16x16x32_f16 v[240:243], v[142:145], v[98:101], v[240:243]
	s_add_u32 m0, s11, 0x22080
	s_nop 0
	global_load_lds_dwordx4 v[228:229], off offset:-128
	v_mfma_f32_16x16x32_f16 v[66:69], v[134:137], v[102:105], v[66:69]
	v_mfma_f32_16x16x32_f16 v[42:45], v[138:141], v[102:105], v[42:45]
	v_mfma_f32_16x16x32_f16 v[236:239], v[142:145], v[102:105], v[236:239]
	v_mfma_f32_16x16x32_f16 v[62:65], v[134:137], v[106:109], v[62:65]
	v_mfma_f32_16x16x32_f16 v[38:41], v[138:141], v[106:109], v[38:41]
	v_mfma_f32_16x16x32_f16 v[34:37], v[142:145], v[106:109], v[34:37]
	s_waitcnt vmcnt(6) lgkmcnt(0)
	s_barrier
	s_add_u32 m0, s11, 0x0
	ds_read_b128 v[134:137], v162 offset:49152
	global_load_lds_dwordx4 v[218:219], off
	v_mfma_f32_16x16x32_f16 v[82:85], v[146:149], v[110:113], v[82:85]
	ds_read_b128 v[138:141], v162 offset:51200
	v_mfma_f32_16x16x32_f16 v[58:61], v[150:153], v[110:113], v[58:61]
	ds_read_b128 v[142:145], v162 offset:53248
	v_mfma_f32_16x16x32_f16 v[14:17], v[154:157], v[110:113], v[14:17]
	ds_read_b128 v[86:89], v158 offset:49152
	v_mfma_f32_16x16x32_f16 v[78:81], v[146:149], v[114:117], v[78:81]
	ds_read_b128 v[90:93], v158 offset:51200
	v_mfma_f32_16x16x32_f16 v[22:25], v[150:153], v[114:117], v[22:25]
	ds_read_b128 v[94:97], v158 offset:53248
	v_mfma_f32_16x16x32_f16 v[30:33], v[154:157], v[114:117], v[30:33]
	s_add_u32 m0, s11, 0x2000
	ds_read_b128 v[98:101], v158 offset:55296
	global_load_lds_dwordx4 v[222:223], off
	v_mfma_f32_16x16x32_f16 v[74:77], v[146:149], v[118:121], v[74:77]
	ds_read_b128 v[102:105], v158 offset:57344
	v_mfma_f32_16x16x32_f16 v[18:21], v[150:153], v[118:121], v[18:21]
	ds_read_b128 v[106:109], v158 offset:59392
	v_mfma_f32_16x16x32_f16 v[26:29], v[154:157], v[118:121], v[26:29]
	v_mfma_f32_16x16x32_f16 v[70:73], v[146:149], v[122:125], v[70:73]
	v_mfma_f32_16x16x32_f16 v[46:49], v[150:153], v[122:125], v[46:49]
	v_mfma_f32_16x16x32_f16 v[240:243], v[154:157], v[122:125], v[240:243]
	s_add_u32 m0, s11, 0x4000
	s_nop 0
	global_load_lds_dwordx4 v[226:227], off
	v_mfma_f32_16x16x32_f16 v[66:69], v[146:149], v[126:129], v[66:69]
	v_mfma_f32_16x16x32_f16 v[42:45], v[150:153], v[126:129], v[42:45]
	v_mfma_f32_16x16x32_f16 v[236:239], v[154:157], v[126:129], v[236:239]
	v_mfma_f32_16x16x32_f16 v[62:65], v[146:149], v[130:133], v[62:65]
	v_mfma_f32_16x16x32_f16 v[38:41], v[150:153], v[130:133], v[38:41]
	v_mfma_f32_16x16x32_f16 v[34:37], v[154:157], v[130:133], v[34:37]
	s_waitcnt lgkmcnt(0)
	s_add_u32 m0, s11, 0x6000
	ds_read_b128 v[146:149], v164 offset:49152
	global_load_lds_dwordx4 v[220:221], off
	v_mfma_f32_16x16x32_f16 v[82:85], v[134:137], v[86:89], v[82:85]
	ds_read_b128 v[150:153], v164 offset:51200
	v_mfma_f32_16x16x32_f16 v[58:61], v[138:141], v[86:89], v[58:61]
	ds_read_b128 v[154:157], v164 offset:53248
	v_mfma_f32_16x16x32_f16 v[14:17], v[142:145], v[86:89], v[14:17]
	ds_read_b128 v[110:113], v160 offset:49152
	v_mfma_f32_16x16x32_f16 v[78:81], v[134:137], v[90:93], v[78:81]
	ds_read_b128 v[114:117], v160 offset:51200
	v_mfma_f32_16x16x32_f16 v[22:25], v[138:141], v[90:93], v[22:25]
	ds_read_b128 v[118:121], v160 offset:53248
	v_mfma_f32_16x16x32_f16 v[30:33], v[142:145], v[90:93], v[30:33]
	s_add_u32 m0, s11, 0x8000
	ds_read_b128 v[122:125], v160 offset:55296
	global_load_lds_dwordx4 v[224:225], off
	v_mfma_f32_16x16x32_f16 v[74:77], v[134:137], v[94:97], v[74:77]
	ds_read_b128 v[126:129], v160 offset:57344
	v_mfma_f32_16x16x32_f16 v[18:21], v[138:141], v[94:97], v[18:21]
	ds_read_b128 v[130:133], v160 offset:59392
	v_mfma_f32_16x16x32_f16 v[26:29], v[142:145], v[94:97], v[26:29]
	v_mfma_f32_16x16x32_f16 v[70:73], v[134:137], v[98:101], v[70:73]
	v_mfma_f32_16x16x32_f16 v[46:49], v[138:141], v[98:101], v[46:49]
	v_mfma_f32_16x16x32_f16 v[240:243], v[142:145], v[98:101], v[240:243]
	s_add_u32 m0, s11, 0xa000
	s_nop 0
	global_load_lds_dwordx4 v[228:229], off
	v_mfma_f32_16x16x32_f16 v[66:69], v[134:137], v[102:105], v[66:69]
	v_mfma_f32_16x16x32_f16 v[42:45], v[138:141], v[102:105], v[42:45]
	v_mfma_f32_16x16x32_f16 v[236:239], v[142:145], v[102:105], v[236:239]
	v_mfma_f32_16x16x32_f16 v[62:65], v[134:137], v[106:109], v[62:65]
	v_mfma_f32_16x16x32_f16 v[38:41], v[138:141], v[106:109], v[38:41]
	v_mfma_f32_16x16x32_f16 v[34:37], v[142:145], v[106:109], v[34:37]
	s_waitcnt vmcnt(6) lgkmcnt(0)
	s_barrier
	s_add_u32 m0, s11, 0xbf80
	ds_read_b128 v[134:137], v163
	global_load_lds_dwordx4 v[218:219], off offset:128
	v_mfma_f32_16x16x32_f16 v[82:85], v[146:149], v[110:113], v[82:85]
	ds_read_b128 v[138:141], v163 offset:2048
	v_mfma_f32_16x16x32_f16 v[58:61], v[150:153], v[110:113], v[58:61]
	ds_read_b128 v[142:145], v163 offset:4096
	v_mfma_f32_16x16x32_f16 v[14:17], v[154:157], v[110:113], v[14:17]
	ds_read_b128 v[86:89], v159
	v_mfma_f32_16x16x32_f16 v[78:81], v[146:149], v[114:117], v[78:81]
	ds_read_b128 v[90:93], v159 offset:2048
	v_mfma_f32_16x16x32_f16 v[22:25], v[150:153], v[114:117], v[22:25]
	ds_read_b128 v[94:97], v159 offset:4096
	v_mfma_f32_16x16x32_f16 v[30:33], v[154:157], v[114:117], v[30:33]
	s_add_u32 m0, s11, 0xdf80
	ds_read_b128 v[98:101], v159 offset:6144
	global_load_lds_dwordx4 v[222:223], off offset:128
	v_mfma_f32_16x16x32_f16 v[74:77], v[146:149], v[118:121], v[74:77]
	ds_read_b128 v[102:105], v159 offset:8192
	v_mfma_f32_16x16x32_f16 v[18:21], v[150:153], v[118:121], v[18:21]
	ds_read_b128 v[106:109], v159 offset:10240
	v_mfma_f32_16x16x32_f16 v[26:29], v[154:157], v[118:121], v[26:29]
	v_mfma_f32_16x16x32_f16 v[70:73], v[146:149], v[122:125], v[70:73]
	v_mfma_f32_16x16x32_f16 v[46:49], v[150:153], v[122:125], v[46:49]
	v_mfma_f32_16x16x32_f16 v[240:243], v[154:157], v[122:125], v[240:243]
	s_add_u32 m0, s11, 0xff80
	s_nop 0
	global_load_lds_dwordx4 v[226:227], off offset:128
	v_mfma_f32_16x16x32_f16 v[66:69], v[146:149], v[126:129], v[66:69]
	v_mfma_f32_16x16x32_f16 v[42:45], v[150:153], v[126:129], v[42:45]
	v_mfma_f32_16x16x32_f16 v[236:239], v[154:157], v[126:129], v[236:239]
	v_mfma_f32_16x16x32_f16 v[62:65], v[146:149], v[130:133], v[62:65]
	v_mfma_f32_16x16x32_f16 v[38:41], v[150:153], v[130:133], v[38:41]
	v_mfma_f32_16x16x32_f16 v[34:37], v[154:157], v[130:133], v[34:37]
	s_waitcnt lgkmcnt(0)
	s_add_u32 m0, s11, 0x11f80
	ds_read_b128 v[146:149], v165
	global_load_lds_dwordx4 v[220:221], off offset:128
	v_mfma_f32_16x16x32_f16 v[82:85], v[134:137], v[86:89], v[82:85]
	ds_read_b128 v[150:153], v165 offset:2048
	v_mfma_f32_16x16x32_f16 v[58:61], v[138:141], v[86:89], v[58:61]
	ds_read_b128 v[154:157], v165 offset:4096
	v_mfma_f32_16x16x32_f16 v[14:17], v[142:145], v[86:89], v[14:17]
	ds_read_b128 v[110:113], v161
	v_mfma_f32_16x16x32_f16 v[78:81], v[134:137], v[90:93], v[78:81]
	ds_read_b128 v[114:117], v161 offset:2048
	v_mfma_f32_16x16x32_f16 v[22:25], v[138:141], v[90:93], v[22:25]
	ds_read_b128 v[118:121], v161 offset:4096
	v_mfma_f32_16x16x32_f16 v[30:33], v[142:145], v[90:93], v[30:33]
	s_add_u32 m0, s11, 0x13f80
	ds_read_b128 v[122:125], v161 offset:6144
	global_load_lds_dwordx4 v[224:225], off offset:128
	v_mfma_f32_16x16x32_f16 v[74:77], v[134:137], v[94:97], v[74:77]
	ds_read_b128 v[126:129], v161 offset:8192
	v_mfma_f32_16x16x32_f16 v[18:21], v[138:141], v[94:97], v[18:21]
	ds_read_b128 v[130:133], v161 offset:10240
	v_mfma_f32_16x16x32_f16 v[26:29], v[142:145], v[94:97], v[26:29]
	v_mfma_f32_16x16x32_f16 v[70:73], v[134:137], v[98:101], v[70:73]
	v_mfma_f32_16x16x32_f16 v[46:49], v[138:141], v[98:101], v[46:49]
	v_mfma_f32_16x16x32_f16 v[240:243], v[142:145], v[98:101], v[240:243]
	s_add_u32 m0, s11, 0x15f80
	s_nop 0
	global_load_lds_dwordx4 v[228:229], off offset:128
	v_mfma_f32_16x16x32_f16 v[66:69], v[134:137], v[102:105], v[66:69]
	v_mfma_f32_16x16x32_f16 v[42:45], v[138:141], v[102:105], v[42:45]
	v_mfma_f32_16x16x32_f16 v[236:239], v[142:145], v[102:105], v[236:239]
	v_mfma_f32_16x16x32_f16 v[62:65], v[134:137], v[106:109], v[62:65]
	v_mfma_f32_16x16x32_f16 v[38:41], v[138:141], v[106:109], v[38:41]
	v_mfma_f32_16x16x32_f16 v[34:37], v[142:145], v[106:109], v[34:37]
	s_waitcnt vmcnt(6) lgkmcnt(0)
	s_barrier
	s_add_u32 m0, s11, 0x17f00
	ds_read_b128 v[134:137], v162
	global_load_lds_dwordx4 v[218:219], off offset:256
	v_mfma_f32_16x16x32_f16 v[82:85], v[146:149], v[110:113], v[82:85]
	ds_read_b128 v[138:141], v162 offset:2048
	v_mfma_f32_16x16x32_f16 v[58:61], v[150:153], v[110:113], v[58:61]
	ds_read_b128 v[142:145], v162 offset:4096
	v_mfma_f32_16x16x32_f16 v[14:17], v[154:157], v[110:113], v[14:17]
	ds_read_b128 v[86:89], v158
	v_mfma_f32_16x16x32_f16 v[78:81], v[146:149], v[114:117], v[78:81]
	ds_read_b128 v[90:93], v158 offset:2048
	v_mfma_f32_16x16x32_f16 v[22:25], v[150:153], v[114:117], v[22:25]
	ds_read_b128 v[94:97], v158 offset:4096
	v_mfma_f32_16x16x32_f16 v[30:33], v[154:157], v[114:117], v[30:33]
	s_add_u32 m0, s11, 0x19f00
	ds_read_b128 v[98:101], v158 offset:6144
	global_load_lds_dwordx4 v[222:223], off offset:256
	v_mfma_f32_16x16x32_f16 v[74:77], v[146:149], v[118:121], v[74:77]
	ds_read_b128 v[102:105], v158 offset:8192
	v_mfma_f32_16x16x32_f16 v[18:21], v[150:153], v[118:121], v[18:21]
	ds_read_b128 v[106:109], v158 offset:10240
	v_mfma_f32_16x16x32_f16 v[26:29], v[154:157], v[118:121], v[26:29]
	v_mfma_f32_16x16x32_f16 v[70:73], v[146:149], v[122:125], v[70:73]
	v_mfma_f32_16x16x32_f16 v[46:49], v[150:153], v[122:125], v[46:49]
	v_mfma_f32_16x16x32_f16 v[240:243], v[154:157], v[122:125], v[240:243]
	s_add_u32 m0, s11, 0x1bf00
	s_nop 0
	global_load_lds_dwordx4 v[226:227], off offset:256
	v_mfma_f32_16x16x32_f16 v[66:69], v[146:149], v[126:129], v[66:69]
	v_mfma_f32_16x16x32_f16 v[42:45], v[150:153], v[126:129], v[42:45]
	v_mfma_f32_16x16x32_f16 v[236:239], v[154:157], v[126:129], v[236:239]
	v_mfma_f32_16x16x32_f16 v[62:65], v[146:149], v[130:133], v[62:65]
	v_mfma_f32_16x16x32_f16 v[38:41], v[150:153], v[130:133], v[38:41]
	v_mfma_f32_16x16x32_f16 v[34:37], v[154:157], v[130:133], v[34:37]
	v_lshl_add_u64 v[218:219], v[218:219], 0, s[20:21]
	v_lshl_add_u64 v[222:223], v[222:223], 0, s[20:21]
	v_lshl_add_u64 v[226:227], v[226:227], 0, s[20:21]
	v_lshl_add_u64 v[220:221], v[220:221], 0, s[20:21]
	v_lshl_add_u64 v[224:225], v[224:225], 0, s[20:21]
	v_lshl_add_u64 v[228:229], v[228:229], 0, s[20:21]
	s_sub_u32 s22, s22, 1
	s_cmp_lg_u32 s22, 0
	s_cbranch_scc1 .Lgemm_T_loop
	s_waitcnt lgkmcnt(0)
	s_add_u32 m0, s11, 0x1e080
	ds_read_b128 v[146:149], v164
	global_load_lds_dwordx4 v[220:221], off offset:-128
	v_mfma_f32_16x16x32_f16 v[82:85], v[134:137], v[86:89], v[82:85]
	ds_read_b128 v[150:153], v164 offset:2048
	v_mfma_f32_16x16x32_f16 v[58:61], v[138:141], v[86:89], v[58:61]
	ds_read_b128 v[154:157], v164 offset:4096
	v_mfma_f32_16x16x32_f16 v[14:17], v[142:145], v[86:89], v[14:17]
	ds_read_b128 v[110:113], v160
	v_mfma_f32_16x16x32_f16 v[78:81], v[134:137], v[90:93], v[78:81]
	ds_read_b128 v[114:117], v160 offset:2048
	v_mfma_f32_16x16x32_f16 v[22:25], v[138:141], v[90:93], v[22:25]
	ds_read_b128 v[118:121], v160 offset:4096
	v_mfma_f32_16x16x32_f16 v[30:33], v[142:145], v[90:93], v[30:33]
	s_add_u32 m0, s11, 0x20080
	ds_read_b128 v[122:125], v160 offset:6144
	global_load_lds_dwordx4 v[224:225], off offset:-128
	v_mfma_f32_16x16x32_f16 v[74:77], v[134:137], v[94:97], v[74:77]
	ds_read_b128 v[126:129], v160 offset:8192
	v_mfma_f32_16x16x32_f16 v[18:21], v[138:141], v[94:97], v[18:21]
	ds_read_b128 v[130:133], v160 offset:10240
	v_mfma_f32_16x16x32_f16 v[26:29], v[142:145], v[94:97], v[26:29]
	v_mfma_f32_16x16x32_f16 v[70:73], v[134:137], v[98:101], v[70:73]
	v_mfma_f32_16x16x32_f16 v[46:49], v[138:141], v[98:101], v[46:49]
	v_mfma_f32_16x16x32_f16 v[240:243], v[142:145], v[98:101], v[240:243]
	s_add_u32 m0, s11, 0x22080
	s_nop 0
	global_load_lds_dwordx4 v[228:229], off offset:-128
	v_mfma_f32_16x16x32_f16 v[66:69], v[134:137], v[102:105], v[66:69]
	v_mfma_f32_16x16x32_f16 v[42:45], v[138:141], v[102:105], v[42:45]
	v_mfma_f32_16x16x32_f16 v[236:239], v[142:145], v[102:105], v[236:239]
	v_mfma_f32_16x16x32_f16 v[62:65], v[134:137], v[106:109], v[62:65]
	v_mfma_f32_16x16x32_f16 v[38:41], v[138:141], v[106:109], v[38:41]
	v_mfma_f32_16x16x32_f16 v[34:37], v[142:145], v[106:109], v[34:37]
	s_waitcnt vmcnt(6) lgkmcnt(0)
	s_barrier
	s_add_u32 m0, s11, 0x0
	ds_read_b128 v[134:137], v162 offset:49152
	global_load_lds_dwordx4 v[218:219], off
	v_mfma_f32_16x16x32_f16 v[82:85], v[146:149], v[110:113], v[82:85]
	ds_read_b128 v[138:141], v162 offset:51200
	v_mfma_f32_16x16x32_f16 v[58:61], v[150:153], v[110:113], v[58:61]
	ds_read_b128 v[142:145], v162 offset:53248
	v_mfma_f32_16x16x32_f16 v[14:17], v[154:157], v[110:113], v[14:17]
	ds_read_b128 v[86:89], v158 offset:49152
	v_mfma_f32_16x16x32_f16 v[78:81], v[146:149], v[114:117], v[78:81]
	ds_read_b128 v[90:93], v158 offset:51200
	v_mfma_f32_16x16x32_f16 v[22:25], v[150:153], v[114:117], v[22:25]
	ds_read_b128 v[94:97], v158 offset:53248
	v_mfma_f32_16x16x32_f16 v[30:33], v[154:157], v[114:117], v[30:33]
	s_add_u32 m0, s11, 0x2000
	ds_read_b128 v[98:101], v158 offset:55296
	global_load_lds_dwordx4 v[222:223], off
	v_mfma_f32_16x16x32_f16 v[74:77], v[146:149], v[118:121], v[74:77]
	ds_read_b128 v[102:105], v158 offset:57344
	v_mfma_f32_16x16x32_f16 v[18:21], v[150:153], v[118:121], v[18:21]
	ds_read_b128 v[106:109], v158 offset:59392
	v_mfma_f32_16x16x32_f16 v[26:29], v[154:157], v[118:121], v[26:29]
	v_mfma_f32_16x16x32_f16 v[70:73], v[146:149], v[122:125], v[70:73]
	v_mfma_f32_16x16x32_f16 v[46:49], v[150:153], v[122:125], v[46:49]
	v_mfma_f32_16x16x32_f16 v[240:243], v[154:157], v[122:125], v[240:243]
	s_add_u32 m0, s11, 0x4000
	s_nop 0
	global_load_lds_dwordx4 v[226:227], off
	v_mfma_f32_16x16x32_f16 v[66:69], v[146:149], v[126:129], v[66:69]
	v_mfma_f32_16x16x32_f16 v[42:45], v[150:153], v[126:129], v[42:45]
	v_mfma_f32_16x16x32_f16 v[236:239], v[154:157], v[126:129], v[236:239]
	v_mfma_f32_16x16x32_f16 v[62:65], v[146:149], v[130:133], v[62:65]
	v_mfma_f32_16x16x32_f16 v[38:41], v[150:153], v[130:133], v[38:41]
	v_mfma_f32_16x16x32_f16 v[34:37], v[154:157], v[130:133], v[34:37]
	s_waitcnt lgkmcnt(0)
	s_add_u32 m0, s11, 0x6000
	ds_read_b128 v[146:149], v164 offset:49152
	global_load_lds_dwordx4 v[220:221], off
	v_mfma_f32_16x16x32_f16 v[82:85], v[134:137], v[86:89], v[82:85]
	ds_read_b128 v[150:153], v164 offset:51200
	v_mfma_f32_16x16x32_f16 v[58:61], v[138:141], v[86:89], v[58:61]
	ds_read_b128 v[154:157], v164 offset:53248
	v_mfma_f32_16x16x32_f16 v[14:17], v[142:145], v[86:89], v[14:17]
	ds_read_b128 v[110:113], v160 offset:49152
	v_mfma_f32_16x16x32_f16 v[78:81], v[134:137], v[90:93], v[78:81]
	ds_read_b128 v[114:117], v160 offset:51200
	v_mfma_f32_16x16x32_f16 v[22:25], v[138:141], v[90:93], v[22:25]
	ds_read_b128 v[118:121], v160 offset:53248
	v_mfma_f32_16x16x32_f16 v[30:33], v[142:145], v[90:93], v[30:33]
	s_add_u32 m0, s11, 0x8000
	ds_read_b128 v[122:125], v160 offset:55296
	global_load_lds_dwordx4 v[224:225], off
	v_mfma_f32_16x16x32_f16 v[74:77], v[134:137], v[94:97], v[74:77]
	ds_read_b128 v[126:129], v160 offset:57344
	v_mfma_f32_16x16x32_f16 v[18:21], v[138:141], v[94:97], v[18:21]
	ds_read_b128 v[130:133], v160 offset:59392
	v_mfma_f32_16x16x32_f16 v[26:29], v[142:145], v[94:97], v[26:29]
	v_mfma_f32_16x16x32_f16 v[70:73], v[134:137], v[98:101], v[70:73]
	v_mfma_f32_16x16x32_f16 v[46:49], v[138:141], v[98:101], v[46:49]
	v_mfma_f32_16x16x32_f16 v[240:243], v[142:145], v[98:101], v[240:243]
	s_add_u32 m0, s11, 0xa000
	s_nop 0
	global_load_lds_dwordx4 v[228:229], off
	v_mfma_f32_16x16x32_f16 v[66:69], v[134:137], v[102:105], v[66:69]
	v_mfma_f32_16x16x32_f16 v[42:45], v[138:141], v[102:105], v[42:45]
	v_mfma_f32_16x16x32_f16 v[236:239], v[142:145], v[102:105], v[236:239]
	v_mfma_f32_16x16x32_f16 v[62:65], v[134:137], v[106:109], v[62:65]
	v_mfma_f32_16x16x32_f16 v[38:41], v[138:141], v[106:109], v[38:41]
	v_mfma_f32_16x16x32_f16 v[34:37], v[142:145], v[106:109], v[34:37]
	s_waitcnt vmcnt(6) lgkmcnt(0)
	s_barrier
	s_lshl_b32 s26, s17, 2
	s_add_u32 s26, s24, s26
	s_addc_u32 s27, s25, 0
	v_lshlrev_b32_e32 v50, 4, v231
	global_load_dwordx4 v[10:13], v50, s[26:27]
	global_load_dwordx4 v[6:9], v50, s[26:27] offset:64
	global_load_dwordx4 v[2:5], v50, s[26:27] offset:128
	ds_read_b128 v[134:137], v163
	v_mfma_f32_16x16x32_f16 v[82:85], v[146:149], v[110:113], v[82:85]
	ds_read_b128 v[138:141], v163 offset:2048
	v_mfma_f32_16x16x32_f16 v[58:61], v[150:153], v[110:113], v[58:61]
	ds_read_b128 v[142:145], v163 offset:4096
	v_mfma_f32_16x16x32_f16 v[14:17], v[154:157], v[110:113], v[14:17]
	ds_read_b128 v[86:89], v159
	v_mfma_f32_16x16x32_f16 v[78:81], v[146:149], v[114:117], v[78:81]
	ds_read_b128 v[90:93], v159 offset:2048
	v_mfma_f32_16x16x32_f16 v[22:25], v[150:153], v[114:117], v[22:25]
	ds_read_b128 v[94:97], v159 offset:4096
	v_mfma_f32_16x16x32_f16 v[30:33], v[154:157], v[114:117], v[30:33]
	ds_read_b128 v[98:101], v159 offset:6144
	v_mfma_f32_16x16x32_f16 v[74:77], v[146:149], v[118:121], v[74:77]
	ds_read_b128 v[102:105], v159 offset:8192
	v_mfma_f32_16x16x32_f16 v[18:21], v[150:153], v[118:121], v[18:21]
	ds_read_b128 v[106:109], v159 offset:10240
	v_mfma_f32_16x16x32_f16 v[26:29], v[154:157], v[118:121], v[26:29]
	v_mfma_f32_16x16x32_f16 v[70:73], v[146:149], v[122:125], v[70:73]
	v_mfma_f32_16x16x32_f16 v[46:49], v[150:153], v[122:125], v[46:49]
	v_mfma_f32_16x16x32_f16 v[240:243], v[154:157], v[122:125], v[240:243]
	v_mfma_f32_16x16x32_f16 v[66:69], v[146:149], v[126:129], v[66:69]
	v_mfma_f32_16x16x32_f16 v[42:45], v[150:153], v[126:129], v[42:45]
	v_mfma_f32_16x16x32_f16 v[236:239], v[154:157], v[126:129], v[236:239]
	v_mfma_f32_16x16x32_f16 v[62:65], v[146:149], v[130:133], v[62:65]
	v_mfma_f32_16x16x32_f16 v[38:41], v[150:153], v[130:133], v[38:41]
	v_mfma_f32_16x16x32_f16 v[34:37], v[154:157], v[130:133], v[34:37]
	s_waitcnt lgkmcnt(0)
	ds_read_b128 v[146:149], v165
	v_mfma_f32_16x16x32_f16 v[82:85], v[134:137], v[86:89], v[82:85]
	ds_read_b128 v[150:153], v165 offset:2048
	v_mfma_f32_16x16x32_f16 v[58:61], v[138:141], v[86:89], v[58:61]
	ds_read_b128 v[154:157], v165 offset:4096
	v_mfma_f32_16x16x32_f16 v[14:17], v[142:145], v[86:89], v[14:17]
	ds_read_b128 v[110:113], v161
	v_mfma_f32_16x16x32_f16 v[78:81], v[134:137], v[90:93], v[78:81]
	ds_read_b128 v[114:117], v161 offset:2048
	v_mfma_f32_16x16x32_f16 v[22:25], v[138:141], v[90:93], v[22:25]
	ds_read_b128 v[118:121], v161 offset:4096
	v_mfma_f32_16x16x32_f16 v[30:33], v[142:145], v[90:93], v[30:33]
	ds_read_b128 v[122:125], v161 offset:6144
	v_mfma_f32_16x16x32_f16 v[74:77], v[134:137], v[94:97], v[74:77]
	ds_read_b128 v[126:129], v161 offset:8192
	v_mfma_f32_16x16x32_f16 v[18:21], v[138:141], v[94:97], v[18:21]
	ds_read_b128 v[130:133], v161 offset:10240
	v_mfma_f32_16x16x32_f16 v[26:29], v[142:145], v[94:97], v[26:29]
	v_mfma_f32_16x16x32_f16 v[70:73], v[134:137], v[98:101], v[70:73]
	v_mfma_f32_16x16x32_f16 v[46:49], v[138:141], v[98:101], v[46:49]
	v_mfma_f32_16x16x32_f16 v[240:243], v[142:145], v[98:101], v[240:243]
	v_mfma_f32_16x16x32_f16 v[66:69], v[134:137], v[102:105], v[66:69]
	v_mfma_f32_16x16x32_f16 v[42:45], v[138:141], v[102:105], v[42:45]
	v_mfma_f32_16x16x32_f16 v[236:239], v[142:145], v[102:105], v[236:239]
	v_mfma_f32_16x16x32_f16 v[62:65], v[134:137], v[106:109], v[62:65]
	v_mfma_f32_16x16x32_f16 v[38:41], v[138:141], v[106:109], v[38:41]
	v_mfma_f32_16x16x32_f16 v[34:37], v[142:145], v[106:109], v[34:37]
	s_waitcnt vmcnt(3) lgkmcnt(0)
	s_barrier
	ds_read_b128 v[134:137], v162
	v_mfma_f32_16x16x32_f16 v[82:85], v[146:149], v[110:113], v[82:85]
	ds_read_b128 v[138:141], v162 offset:2048
	v_mfma_f32_16x16x32_f16 v[58:61], v[150:153], v[110:113], v[58:61]
	ds_read_b128 v[142:145], v162 offset:4096
	v_mfma_f32_16x16x32_f16 v[14:17], v[154:157], v[110:113], v[14:17]
	ds_read_b128 v[86:89], v158
	v_mfma_f32_16x16x32_f16 v[78:81], v[146:149], v[114:117], v[78:81]
	ds_read_b128 v[90:93], v158 offset:2048
	v_mfma_f32_16x16x32_f16 v[22:25], v[150:153], v[114:117], v[22:25]
	ds_read_b128 v[94:97], v158 offset:4096
	v_mfma_f32_16x16x32_f16 v[30:33], v[154:157], v[114:117], v[30:33]
	ds_read_b128 v[98:101], v158 offset:6144
	v_mfma_f32_16x16x32_f16 v[74:77], v[146:149], v[118:121], v[74:77]
	ds_read_b128 v[102:105], v158 offset:8192
	v_mfma_f32_16x16x32_f16 v[18:21], v[150:153], v[118:121], v[18:21]
	ds_read_b128 v[106:109], v158 offset:10240
	v_mfma_f32_16x16x32_f16 v[26:29], v[154:157], v[118:121], v[26:29]
	v_mfma_f32_16x16x32_f16 v[70:73], v[146:149], v[122:125], v[70:73]
	v_mfma_f32_16x16x32_f16 v[46:49], v[150:153], v[122:125], v[46:49]
	v_mfma_f32_16x16x32_f16 v[240:243], v[154:157], v[122:125], v[240:243]
	v_mfma_f32_16x16x32_f16 v[66:69], v[146:149], v[126:129], v[66:69]
	v_mfma_f32_16x16x32_f16 v[42:45], v[150:153], v[126:129], v[42:45]
	v_mfma_f32_16x16x32_f16 v[236:239], v[154:157], v[126:129], v[236:239]
	v_mfma_f32_16x16x32_f16 v[62:65], v[146:149], v[130:133], v[62:65]
	v_mfma_f32_16x16x32_f16 v[38:41], v[150:153], v[130:133], v[38:41]
	v_mfma_f32_16x16x32_f16 v[34:37], v[154:157], v[130:133], v[34:37]
	s_waitcnt lgkmcnt(0)
	ds_read_b128 v[146:149], v164
	v_mfma_f32_16x16x32_f16 v[82:85], v[134:137], v[86:89], v[82:85]
	ds_read_b128 v[150:153], v164 offset:2048
	v_mfma_f32_16x16x32_f16 v[58:61], v[138:141], v[86:89], v[58:61]
	ds_read_b128 v[154:157], v164 offset:4096
	v_mfma_f32_16x16x32_f16 v[14:17], v[142:145], v[86:89], v[14:17]
	ds_read_b128 v[110:113], v160
	v_mfma_f32_16x16x32_f16 v[78:81], v[134:137], v[90:93], v[78:81]
	ds_read_b128 v[114:117], v160 offset:2048
	v_mfma_f32_16x16x32_f16 v[22:25], v[138:141], v[90:93], v[22:25]
	ds_read_b128 v[118:121], v160 offset:4096
	v_mfma_f32_16x16x32_f16 v[30:33], v[142:145], v[90:93], v[30:33]
	ds_read_b128 v[122:125], v160 offset:6144
	v_mfma_f32_16x16x32_f16 v[74:77], v[134:137], v[94:97], v[74:77]
	ds_read_b128 v[126:129], v160 offset:8192
	v_mfma_f32_16x16x32_f16 v[18:21], v[138:141], v[94:97], v[18:21]
	ds_read_b128 v[130:133], v160 offset:10240
	v_mfma_f32_16x16x32_f16 v[26:29], v[142:145], v[94:97], v[26:29]
	v_mfma_f32_16x16x32_f16 v[70:73], v[134:137], v[98:101], v[70:73]
	v_mfma_f32_16x16x32_f16 v[46:49], v[138:141], v[98:101], v[46:49]
	v_mfma_f32_16x16x32_f16 v[240:243], v[142:145], v[98:101], v[240:243]
	v_mfma_f32_16x16x32_f16 v[66:69], v[134:137], v[102:105], v[66:69]
	v_mfma_f32_16x16x32_f16 v[42:45], v[138:141], v[102:105], v[42:45]
	v_mfma_f32_16x16x32_f16 v[236:239], v[142:145], v[102:105], v[236:239]
	v_mfma_f32_16x16x32_f16 v[62:65], v[134:137], v[106:109], v[62:65]
	v_mfma_f32_16x16x32_f16 v[38:41], v[138:141], v[106:109], v[38:41]
	v_mfma_f32_16x16x32_f16 v[34:37], v[142:145], v[106:109], v[34:37]
	s_waitcnt lgkmcnt(0)
	v_mfma_f32_16x16x32_f16 v[82:85], v[146:149], v[110:113], v[82:85]
	v_mfma_f32_16x16x32_f16 v[58:61], v[150:153], v[110:113], v[58:61]
	v_mfma_f32_16x16x32_f16 v[14:17], v[154:157], v[110:113], v[14:17]
	v_mfma_f32_16x16x32_f16 v[78:81], v[146:149], v[114:117], v[78:81]
	v_mfma_f32_16x16x32_f16 v[22:25], v[150:153], v[114:117], v[22:25]
	v_mfma_f32_16x16x32_f16 v[30:33], v[154:157], v[114:117], v[30:33]
	v_mfma_f32_16x16x32_f16 v[74:77], v[146:149], v[118:121], v[74:77]
	v_mfma_f32_16x16x32_f16 v[18:21], v[150:153], v[118:121], v[18:21]
	v_mfma_f32_16x16x32_f16 v[26:29], v[154:157], v[118:121], v[26:29]
	v_mfma_f32_16x16x32_f16 v[70:73], v[146:149], v[122:125], v[70:73]
	v_mfma_f32_16x16x32_f16 v[46:49], v[150:153], v[122:125], v[46:49]
	v_mfma_f32_16x16x32_f16 v[240:243], v[154:157], v[122:125], v[240:243]
	v_mfma_f32_16x16x32_f16 v[66:69], v[146:149], v[126:129], v[66:69]
	v_mfma_f32_16x16x32_f16 v[42:45], v[150:153], v[126:129], v[42:45]
	v_mfma_f32_16x16x32_f16 v[236:239], v[154:157], v[126:129], v[236:239]
	v_mfma_f32_16x16x32_f16 v[62:65], v[146:149], v[130:133], v[62:65]
	v_mfma_f32_16x16x32_f16 v[38:41], v[150:153], v[130:133], v[38:41]
	v_mfma_f32_16x16x32_f16 v[34:37], v[154:157], v[130:133], v[34:37]
	s_branch .LBB1_76
.Lgemm_N_loop:
	s_waitcnt lgkmcnt(0)
	s_add_u32 m0, s11, 0x1e080
	ds_read_b128 v[146:149], v164
	global_load_lds_dwordx4 v[220:221], off offset:-128
	v_mfma_f32_16x16x32_f16 v[82:85], v[86:89], v[134:137], v[82:85]
	ds_read_b128 v[150:153], v164 offset:2048
	v_mfma_f32_16x16x32_f16 v[58:61], v[86:89], v[138:141], v[58:61]
	ds_read_b128 v[154:157], v164 offset:4096
	v_mfma_f32_16x16x32_f16 v[14:17], v[86:89], v[142:145], v[14:17]
	ds_read_b128 v[110:113], v160
	v_mfma_f32_16x16x32_f16 v[78:81], v[90:93], v[134:137], v[78:81]
	ds_read_b128 v[114:117], v160 offset:2048
	v_mfma_f32_16x16x32_f16 v[22:25], v[90:93], v[138:141], v[22:25]
	ds_read_b128 v[118:121], v160 offset:4096
	v_mfma_f32_16x16x32_f16 v[30:33], v[90:93], v[142:145], v[30:33]
	s_add_u32 m0, s11, 0x20080
	ds_read_b128 v[122:125], v160 offset:6144
	global_load_lds_dwordx4 v[224:225], off offset:-128
	v_mfma_f32_16x16x32_f16 v[74:77], v[94:97], v[134:137], v[74:77]
	ds_read_b128 v[126:129], v160 offset:8192
	v_mfma_f32_16x16x32_f16 v[18:21], v[94:97], v[138:141], v[18:21]
	ds_read_b128 v[130:133], v160 offset:10240
	v_mfma_f32_16x16x32_f16 v[26:29], v[94:97], v[142:145], v[26:29]
	v_mfma_f32_16x16x32_f16 v[70:73], v[98:101], v[134:137], v[70:73]
	v_mfma_f32_16x16x32_f16 v[46:49], v[98:101], v[138:141], v[46:49]
	v_mfma_f32_16x16x32_f16 v[240:243], v[98:101], v[142:145], v[240:243]
	s_add_u32 m0, s11, 0x22080
	s_nop 0
	global_load_lds_dwordx4 v[228:229], off offset:-128
	v_mfma_f32_16x16x32_f16 v[66:69], v[102:105], v[134:137], v[66:69]
	v_mfma_f32_16x16x32_f16 v[42:45], v[102:105], v[138:141], v[42:45]
	v_mfma_f32_16x16x32_f16 v[236:239], v[102:105], v[142:145], v[236:239]
	v_mfma_f32_16x16x32_f16 v[62:65], v[106:109], v[134:137], v[62:65]
	v_mfma_f32_16x16x32_f16 v[38:41], v[106:109], v[138:141], v[38:41]
	v_mfma_f32_16x16x32_f16 v[34:37], v[106:109], v[142:145], v[34:37]
	s_waitcnt vmcnt(6) lgkmcnt(0)
	s_barrier
	s_add_u32 m0, s11, 0x0
	ds_read_b128 v[134:137], v162 offset:49152
	global_load_lds_dwordx4 v[218:219], off
	v_mfma_f32_16x16x32_f16 v[82:85], v[110:113], v[146:149], v[82:85]
	ds_read_b128 v[138:141], v162 offset:51200
	v_mfma_f32_16x16x32_f16 v[58:61], v[110:113], v[150:153], v[58:61]
	ds_read_b128 v[142:145], v162 offset:53248
	v_mfma_f32_16x16x32_f16 v[14:17], v[110:113], v[154:157], v[14:17]
	ds_read_b128 v[86:89], v158 offset:49152
	v_mfma_f32_16x16x32_f16 v[78:81], v[114:117], v[146:149], v[78:81]
	ds_read_b128 v[90:93], v158 offset:51200
	v_mfma_f32_16x16x32_f16 v[22:25], v[114:117], v[150:153], v[22:25]
	ds_read_b128 v[94:97], v158 offset:53248
	v_mfma_f32_16x16x32_f16 v[30:33], v[114:117], v[154:157], v[30:33]
	s_add_u32 m0, s11, 0x2000
	ds_read_b128 v[98:101], v158 offset:55296
	global_load_lds_dwordx4 v[222:223], off
	v_mfma_f32_16x16x32_f16 v[74:77], v[118:121], v[146:149], v[74:77]
	ds_read_b128 v[102:105], v158 offset:57344
	v_mfma_f32_16x16x32_f16 v[18:21], v[118:121], v[150:153], v[18:21]
	ds_read_b128 v[106:109], v158 offset:59392
	v_mfma_f32_16x16x32_f16 v[26:29], v[118:121], v[154:157], v[26:29]
	v_mfma_f32_16x16x32_f16 v[70:73], v[122:125], v[146:149], v[70:73]
	v_mfma_f32_16x16x32_f16 v[46:49], v[122:125], v[150:153], v[46:49]
	v_mfma_f32_16x16x32_f16 v[240:243], v[122:125], v[154:157], v[240:243]
	s_add_u32 m0, s11, 0x4000
	s_nop 0
	global_load_lds_dwordx4 v[226:227], off
	v_mfma_f32_16x16x32_f16 v[66:69], v[126:129], v[146:149], v[66:69]
	v_mfma_f32_16x16x32_f16 v[42:45], v[126:129], v[150:153], v[42:45]
	v_mfma_f32_16x16x32_f16 v[236:239], v[126:129], v[154:157], v[236:239]
	v_mfma_f32_16x16x32_f16 v[62:65], v[130:133], v[146:149], v[62:65]
	v_mfma_f32_16x16x32_f16 v[38:41], v[130:133], v[150:153], v[38:41]
	v_mfma_f32_16x16x32_f16 v[34:37], v[130:133], v[154:157], v[34:37]
	s_waitcnt lgkmcnt(0)
	s_add_u32 m0, s11, 0x6000
	ds_read_b128 v[146:149], v164 offset:49152
	global_load_lds_dwordx4 v[220:221], off
	v_mfma_f32_16x16x32_f16 v[82:85], v[86:89], v[134:137], v[82:85]
	ds_read_b128 v[150:153], v164 offset:51200
	v_mfma_f32_16x16x32_f16 v[58:61], v[86:89], v[138:141], v[58:61]
	ds_read_b128 v[154:157], v164 offset:53248
	v_mfma_f32_16x16x32_f16 v[14:17], v[86:89], v[142:145], v[14:17]
	ds_read_b128 v[110:113], v160 offset:49152
	v_mfma_f32_16x16x32_f16 v[78:81], v[90:93], v[134:137], v[78:81]
	ds_read_b128 v[114:117], v160 offset:51200
	v_mfma_f32_16x16x32_f16 v[22:25], v[90:93], v[138:141], v[22:25]
	ds_read_b128 v[118:121], v160 offset:53248
	v_mfma_f32_16x16x32_f16 v[30:33], v[90:93], v[142:145], v[30:33]
	s_add_u32 m0, s11, 0x8000
	ds_read_b128 v[122:125], v160 offset:55296
	global_load_lds_dwordx4 v[224:225], off
	v_mfma_f32_16x16x32_f16 v[74:77], v[94:97], v[134:137], v[74:77]
	ds_read_b128 v[126:129], v160 offset:57344
	v_mfma_f32_16x16x32_f16 v[18:21], v[94:97], v[138:141], v[18:21]
	ds_read_b128 v[130:133], v160 offset:59392
	v_mfma_f32_16x16x32_f16 v[26:29], v[94:97], v[142:145], v[26:29]
	v_mfma_f32_16x16x32_f16 v[70:73], v[98:101], v[134:137], v[70:73]
	v_mfma_f32_16x16x32_f16 v[46:49], v[98:101], v[138:141], v[46:49]
	v_mfma_f32_16x16x32_f16 v[240:243], v[98:101], v[142:145], v[240:243]
	s_add_u32 m0, s11, 0xa000
	s_nop 0
	global_load_lds_dwordx4 v[228:229], off
	v_mfma_f32_16x16x32_f16 v[66:69], v[102:105], v[134:137], v[66:69]
	v_mfma_f32_16x16x32_f16 v[42:45], v[102:105], v[138:141], v[42:45]
	v_mfma_f32_16x16x32_f16 v[236:239], v[102:105], v[142:145], v[236:239]
	v_mfma_f32_16x16x32_f16 v[62:65], v[106:109], v[134:137], v[62:65]
	v_mfma_f32_16x16x32_f16 v[38:41], v[106:109], v[138:141], v[38:41]
	v_mfma_f32_16x16x32_f16 v[34:37], v[106:109], v[142:145], v[34:37]
	s_waitcnt vmcnt(6) lgkmcnt(0)
	s_barrier
	s_add_u32 m0, s11, 0xbf80
	ds_read_b128 v[134:137], v163
	global_load_lds_dwordx4 v[218:219], off offset:128
	v_mfma_f32_16x16x32_f16 v[82:85], v[110:113], v[146:149], v[82:85]
	ds_read_b128 v[138:141], v163 offset:2048
	v_mfma_f32_16x16x32_f16 v[58:61], v[110:113], v[150:153], v[58:61]
	ds_read_b128 v[142:145], v163 offset:4096
	v_mfma_f32_16x16x32_f16 v[14:17], v[110:113], v[154:157], v[14:17]
	ds_read_b128 v[86:89], v159
	v_mfma_f32_16x16x32_f16 v[78:81], v[114:117], v[146:149], v[78:81]
	ds_read_b128 v[90:93], v159 offset:2048
	v_mfma_f32_16x16x32_f16 v[22:25], v[114:117], v[150:153], v[22:25]
	ds_read_b128 v[94:97], v159 offset:4096
	v_mfma_f32_16x16x32_f16 v[30:33], v[114:117], v[154:157], v[30:33]
	s_add_u32 m0, s11, 0xdf80
	ds_read_b128 v[98:101], v159 offset:6144
	global_load_lds_dwordx4 v[222:223], off offset:128
	v_mfma_f32_16x16x32_f16 v[74:77], v[118:121], v[146:149], v[74:77]
	ds_read_b128 v[102:105], v159 offset:8192
	v_mfma_f32_16x16x32_f16 v[18:21], v[118:121], v[150:153], v[18:21]
	ds_read_b128 v[106:109], v159 offset:10240
	v_mfma_f32_16x16x32_f16 v[26:29], v[118:121], v[154:157], v[26:29]
	v_mfma_f32_16x16x32_f16 v[70:73], v[122:125], v[146:149], v[70:73]
	v_mfma_f32_16x16x32_f16 v[46:49], v[122:125], v[150:153], v[46:49]
	v_mfma_f32_16x16x32_f16 v[240:243], v[122:125], v[154:157], v[240:243]
	s_add_u32 m0, s11, 0xff80
	s_nop 0
	global_load_lds_dwordx4 v[226:227], off offset:128
	v_mfma_f32_16x16x32_f16 v[66:69], v[126:129], v[146:149], v[66:69]
	v_mfma_f32_16x16x32_f16 v[42:45], v[126:129], v[150:153], v[42:45]
	v_mfma_f32_16x16x32_f16 v[236:239], v[126:129], v[154:157], v[236:239]
	v_mfma_f32_16x16x32_f16 v[62:65], v[130:133], v[146:149], v[62:65]
	v_mfma_f32_16x16x32_f16 v[38:41], v[130:133], v[150:153], v[38:41]
	v_mfma_f32_16x16x32_f16 v[34:37], v[130:133], v[154:157], v[34:37]
	s_waitcnt lgkmcnt(0)
	s_add_u32 m0, s11, 0x11f80
	ds_read_b128 v[146:149], v165
	global_load_lds_dwordx4 v[220:221], off offset:128
	v_mfma_f32_16x16x32_f16 v[82:85], v[86:89], v[134:137], v[82:85]
	ds_read_b128 v[150:153], v165 offset:2048
	v_mfma_f32_16x16x32_f16 v[58:61], v[86:89], v[138:141], v[58:61]
	ds_read_b128 v[154:157], v165 offset:4096
	v_mfma_f32_16x16x32_f16 v[14:17], v[86:89], v[142:145], v[14:17]
	ds_read_b128 v[110:113], v161
	v_mfma_f32_16x16x32_f16 v[78:81], v[90:93], v[134:137], v[78:81]
	ds_read_b128 v[114:117], v161 offset:2048
	v_mfma_f32_16x16x32_f16 v[22:25], v[90:93], v[138:141], v[22:25]
	ds_read_b128 v[118:121], v161 offset:4096
	v_mfma_f32_16x16x32_f16 v[30:33], v[90:93], v[142:145], v[30:33]
	s_add_u32 m0, s11, 0x13f80
	ds_read_b128 v[122:125], v161 offset:6144
	global_load_lds_dwordx4 v[224:225], off offset:128
	v_mfma_f32_16x16x32_f16 v[74:77], v[94:97], v[134:137], v[74:77]
	ds_read_b128 v[126:129], v161 offset:8192
	v_mfma_f32_16x16x32_f16 v[18:21], v[94:97], v[138:141], v[18:21]
	ds_read_b128 v[130:133], v161 offset:10240
	v_mfma_f32_16x16x32_f16 v[26:29], v[94:97], v[142:145], v[26:29]
	v_mfma_f32_16x16x32_f16 v[70:73], v[98:101], v[134:137], v[70:73]
	v_mfma_f32_16x16x32_f16 v[46:49], v[98:101], v[138:141], v[46:49]
	v_mfma_f32_16x16x32_f16 v[240:243], v[98:101], v[142:145], v[240:243]
	s_add_u32 m0, s11, 0x15f80
	s_nop 0
	global_load_lds_dwordx4 v[228:229], off offset:128
	v_mfma_f32_16x16x32_f16 v[66:69], v[102:105], v[134:137], v[66:69]
	v_mfma_f32_16x16x32_f16 v[42:45], v[102:105], v[138:141], v[42:45]
	v_mfma_f32_16x16x32_f16 v[236:239], v[102:105], v[142:145], v[236:239]
	v_mfma_f32_16x16x32_f16 v[62:65], v[106:109], v[134:137], v[62:65]
	v_mfma_f32_16x16x32_f16 v[38:41], v[106:109], v[138:141], v[38:41]
	v_mfma_f32_16x16x32_f16 v[34:37], v[106:109], v[142:145], v[34:37]
	s_waitcnt vmcnt(6) lgkmcnt(0)
	s_barrier
	s_add_u32 m0, s11, 0x17f00
	ds_read_b128 v[134:137], v162
	global_load_lds_dwordx4 v[218:219], off offset:256
	v_mfma_f32_16x16x32_f16 v[82:85], v[110:113], v[146:149], v[82:85]
	ds_read_b128 v[138:141], v162 offset:2048
	v_mfma_f32_16x16x32_f16 v[58:61], v[110:113], v[150:153], v[58:61]
	ds_read_b128 v[142:145], v162 offset:4096
	v_mfma_f32_16x16x32_f16 v[14:17], v[110:113], v[154:157], v[14:17]
	ds_read_b128 v[86:89], v158
	v_mfma_f32_16x16x32_f16 v[78:81], v[114:117], v[146:149], v[78:81]
	ds_read_b128 v[90:93], v158 offset:2048
	v_mfma_f32_16x16x32_f16 v[22:25], v[114:117], v[150:153], v[22:25]
	ds_read_b128 v[94:97], v158 offset:4096
	v_mfma_f32_16x16x32_f16 v[30:33], v[114:117], v[154:157], v[30:33]
	s_add_u32 m0, s11, 0x19f00
	ds_read_b128 v[98:101], v158 offset:6144
	global_load_lds_dwordx4 v[222:223], off offset:256
	v_mfma_f32_16x16x32_f16 v[74:77], v[118:121], v[146:149], v[74:77]
	ds_read_b128 v[102:105], v158 offset:8192
	v_mfma_f32_16x16x32_f16 v[18:21], v[118:121], v[150:153], v[18:21]
	ds_read_b128 v[106:109], v158 offset:10240
	v_mfma_f32_16x16x32_f16 v[26:29], v[118:121], v[154:157], v[26:29]
	v_mfma_f32_16x16x32_f16 v[70:73], v[122:125], v[146:149], v[70:73]
	v_mfma_f32_16x16x32_f16 v[46:49], v[122:125], v[150:153], v[46:49]
	v_mfma_f32_16x16x32_f16 v[240:243], v[122:125], v[154:157], v[240:243]
	s_add_u32 m0, s11, 0x1bf00
	s_nop 0
	global_load_lds_dwordx4 v[226:227], off offset:256
	v_mfma_f32_16x16x32_f16 v[66:69], v[126:129], v[146:149], v[66:69]
	v_mfma_f32_16x16x32_f16 v[42:45], v[126:129], v[150:153], v[42:45]
	v_mfma_f32_16x16x32_f16 v[236:239], v[126:129], v[154:157], v[236:239]
	v_mfma_f32_16x16x32_f16 v[62:65], v[130:133], v[146:149], v[62:65]
	v_mfma_f32_16x16x32_f16 v[38:41], v[130:133], v[150:153], v[38:41]
	v_mfma_f32_16x16x32_f16 v[34:37], v[130:133], v[154:157], v[34:37]
	v_lshl_add_u64 v[218:219], v[218:219], 0, s[20:21]
	v_lshl_add_u64 v[222:223], v[222:223], 0, s[20:21]
	v_lshl_add_u64 v[226:227], v[226:227], 0, s[20:21]
	v_lshl_add_u64 v[220:221], v[220:221], 0, s[20:21]
	v_lshl_add_u64 v[224:225], v[224:225], 0, s[20:21]
	v_lshl_add_u64 v[228:229], v[228:229], 0, s[20:21]
	s_sub_u32 s22, s22, 1
	s_cmp_lg_u32 s22, 0
	s_cbranch_scc1 .Lgemm_N_loop
	s_waitcnt lgkmcnt(0)
	s_add_u32 m0, s11, 0x1e080
	ds_read_b128 v[146:149], v164
	global_load_lds_dwordx4 v[220:221], off offset:-128
	v_mfma_f32_16x16x32_f16 v[82:85], v[86:89], v[134:137], v[82:85]
	ds_read_b128 v[150:153], v164 offset:2048
	v_mfma_f32_16x16x32_f16 v[58:61], v[86:89], v[138:141], v[58:61]
	ds_read_b128 v[154:157], v164 offset:4096
	v_mfma_f32_16x16x32_f16 v[14:17], v[86:89], v[142:145], v[14:17]
	ds_read_b128 v[110:113], v160
	v_mfma_f32_16x16x32_f16 v[78:81], v[90:93], v[134:137], v[78:81]
	ds_read_b128 v[114:117], v160 offset:2048
	v_mfma_f32_16x16x32_f16 v[22:25], v[90:93], v[138:141], v[22:25]
	ds_read_b128 v[118:121], v160 offset:4096
	v_mfma_f32_16x16x32_f16 v[30:33], v[90:93], v[142:145], v[30:33]
	s_add_u32 m0, s11, 0x20080
	ds_read_b128 v[122:125], v160 offset:6144
	global_load_lds_dwordx4 v[224:225], off offset:-128
	v_mfma_f32_16x16x32_f16 v[74:77], v[94:97], v[134:137], v[74:77]
	ds_read_b128 v[126:129], v160 offset:8192
	v_mfma_f32_16x16x32_f16 v[18:21], v[94:97], v[138:141], v[18:21]
	ds_read_b128 v[130:133], v160 offset:10240
	v_mfma_f32_16x16x32_f16 v[26:29], v[94:97], v[142:145], v[26:29]
	v_mfma_f32_16x16x32_f16 v[70:73], v[98:101], v[134:137], v[70:73]
	v_mfma_f32_16x16x32_f16 v[46:49], v[98:101], v[138:141], v[46:49]
	v_mfma_f32_16x16x32_f16 v[240:243], v[98:101], v[142:145], v[240:243]
	s_add_u32 m0, s11, 0x22080
	s_nop 0
	global_load_lds_dwordx4 v[228:229], off offset:-128
	v_mfma_f32_16x16x32_f16 v[66:69], v[102:105], v[134:137], v[66:69]
	v_mfma_f32_16x16x32_f16 v[42:45], v[102:105], v[138:141], v[42:45]
	v_mfma_f32_16x16x32_f16 v[236:239], v[102:105], v[142:145], v[236:239]
	v_mfma_f32_16x16x32_f16 v[62:65], v[106:109], v[134:137], v[62:65]
	v_mfma_f32_16x16x32_f16 v[38:41], v[106:109], v[138:141], v[38:41]
	v_mfma_f32_16x16x32_f16 v[34:37], v[106:109], v[142:145], v[34:37]
	s_waitcnt vmcnt(6) lgkmcnt(0)
	s_barrier
	s_add_u32 m0, s11, 0x0
	ds_read_b128 v[134:137], v162 offset:49152
	global_load_lds_dwordx4 v[218:219], off
	v_mfma_f32_16x16x32_f16 v[82:85], v[110:113], v[146:149], v[82:85]
	ds_read_b128 v[138:141], v162 offset:51200
	v_mfma_f32_16x16x32_f16 v[58:61], v[110:113], v[150:153], v[58:61]
	ds_read_b128 v[142:145], v162 offset:53248
	v_mfma_f32_16x16x32_f16 v[14:17], v[110:113], v[154:157], v[14:17]
	ds_read_b128 v[86:89], v158 offset:49152
	v_mfma_f32_16x16x32_f16 v[78:81], v[114:117], v[146:149], v[78:81]
	ds_read_b128 v[90:93], v158 offset:51200
	v_mfma_f32_16x16x32_f16 v[22:25], v[114:117], v[150:153], v[22:25]
	ds_read_b128 v[94:97], v158 offset:53248
	v_mfma_f32_16x16x32_f16 v[30:33], v[114:117], v[154:157], v[30:33]
	s_add_u32 m0, s11, 0x2000
	ds_read_b128 v[98:101], v158 offset:55296
	global_load_lds_dwordx4 v[222:223], off
	v_mfma_f32_16x16x32_f16 v[74:77], v[118:121], v[146:149], v[74:77]
	ds_read_b128 v[102:105], v158 offset:57344
	v_mfma_f32_16x16x32_f16 v[18:21], v[118:121], v[150:153], v[18:21]
	ds_read_b128 v[106:109], v158 offset:59392
	v_mfma_f32_16x16x32_f16 v[26:29], v[118:121], v[154:157], v[26:29]
	v_mfma_f32_16x16x32_f16 v[70:73], v[122:125], v[146:149], v[70:73]
	v_mfma_f32_16x16x32_f16 v[46:49], v[122:125], v[150:153], v[46:49]
	v_mfma_f32_16x16x32_f16 v[240:243], v[122:125], v[154:157], v[240:243]
	s_add_u32 m0, s11, 0x4000
	s_nop 0
	global_load_lds_dwordx4 v[226:227], off
	v_mfma_f32_16x16x32_f16 v[66:69], v[126:129], v[146:149], v[66:69]
	v_mfma_f32_16x16x32_f16 v[42:45], v[126:129], v[150:153], v[42:45]
	v_mfma_f32_16x16x32_f16 v[236:239], v[126:129], v[154:157], v[236:239]
	v_mfma_f32_16x16x32_f16 v[62:65], v[130:133], v[146:149], v[62:65]
	v_mfma_f32_16x16x32_f16 v[38:41], v[130:133], v[150:153], v[38:41]
	v_mfma_f32_16x16x32_f16 v[34:37], v[130:133], v[154:157], v[34:37]
	s_waitcnt lgkmcnt(0)
	s_add_u32 m0, s11, 0x6000
	ds_read_b128 v[146:149], v164 offset:49152
	global_load_lds_dwordx4 v[220:221], off
	v_mfma_f32_16x16x32_f16 v[82:85], v[86:89], v[134:137], v[82:85]
	ds_read_b128 v[150:153], v164 offset:51200
	v_mfma_f32_16x16x32_f16 v[58:61], v[86:89], v[138:141], v[58:61]
	ds_read_b128 v[154:157], v164 offset:53248
	v_mfma_f32_16x16x32_f16 v[14:17], v[86:89], v[142:145], v[14:17]
	ds_read_b128 v[110:113], v160 offset:49152
	v_mfma_f32_16x16x32_f16 v[78:81], v[90:93], v[134:137], v[78:81]
	ds_read_b128 v[114:117], v160 offset:51200
	v_mfma_f32_16x16x32_f16 v[22:25], v[90:93], v[138:141], v[22:25]
	ds_read_b128 v[118:121], v160 offset:53248
	v_mfma_f32_16x16x32_f16 v[30:33], v[90:93], v[142:145], v[30:33]
	s_add_u32 m0, s11, 0x8000
	ds_read_b128 v[122:125], v160 offset:55296
	global_load_lds_dwordx4 v[224:225], off
	v_mfma_f32_16x16x32_f16 v[74:77], v[94:97], v[134:137], v[74:77]
	ds_read_b128 v[126:129], v160 offset:57344
	v_mfma_f32_16x16x32_f16 v[18:21], v[94:97], v[138:141], v[18:21]
	ds_read_b128 v[130:133], v160 offset:59392
	v_mfma_f32_16x16x32_f16 v[26:29], v[94:97], v[142:145], v[26:29]
	v_mfma_f32_16x16x32_f16 v[70:73], v[98:101], v[134:137], v[70:73]
	v_mfma_f32_16x16x32_f16 v[46:49], v[98:101], v[138:141], v[46:49]
	v_mfma_f32_16x16x32_f16 v[240:243], v[98:101], v[142:145], v[240:243]
	s_add_u32 m0, s11, 0xa000
	s_nop 0
	global_load_lds_dwordx4 v[228:229], off
	v_mfma_f32_16x16x32_f16 v[66:69], v[102:105], v[134:137], v[66:69]
	v_mfma_f32_16x16x32_f16 v[42:45], v[102:105], v[138:141], v[42:45]
	v_mfma_f32_16x16x32_f16 v[236:239], v[102:105], v[142:145], v[236:239]
	v_mfma_f32_16x16x32_f16 v[62:65], v[106:109], v[134:137], v[62:65]
	v_mfma_f32_16x16x32_f16 v[38:41], v[106:109], v[138:141], v[38:41]
	v_mfma_f32_16x16x32_f16 v[34:37], v[106:109], v[142:145], v[34:37]
	s_waitcnt vmcnt(6) lgkmcnt(0)
	s_barrier
	s_lshl_b32 s26, s17, 2
	s_add_u32 s26, s24, s26
	s_addc_u32 s27, s25, 0
	v_lshlrev_b32_e32 v50, 2, v1
	global_load_dword v234, v50, s[26:27]
	global_load_dword v232, v50, s[26:27] offset:64
	global_load_dword v230, v50, s[26:27] offset:128
	ds_read_b128 v[134:137], v163
	v_mfma_f32_16x16x32_f16 v[82:85], v[110:113], v[146:149], v[82:85]
	ds_read_b128 v[138:141], v163 offset:2048
	v_mfma_f32_16x16x32_f16 v[58:61], v[110:113], v[150:153], v[58:61]
	ds_read_b128 v[142:145], v163 offset:4096
	v_mfma_f32_16x16x32_f16 v[14:17], v[110:113], v[154:157], v[14:17]
	ds_read_b128 v[86:89], v159
	v_mfma_f32_16x16x32_f16 v[78:81], v[114:117], v[146:149], v[78:81]
	ds_read_b128 v[90:93], v159 offset:2048
	v_mfma_f32_16x16x32_f16 v[22:25], v[114:117], v[150:153], v[22:25]
	ds_read_b128 v[94:97], v159 offset:4096
	v_mfma_f32_16x16x32_f16 v[30:33], v[114:117], v[154:157], v[30:33]
	ds_read_b128 v[98:101], v159 offset:6144
	v_mfma_f32_16x16x32_f16 v[74:77], v[118:121], v[146:149], v[74:77]
	ds_read_b128 v[102:105], v159 offset:8192
	v_mfma_f32_16x16x32_f16 v[18:21], v[118:121], v[150:153], v[18:21]
	ds_read_b128 v[106:109], v159 offset:10240
	v_mfma_f32_16x16x32_f16 v[26:29], v[118:121], v[154:157], v[26:29]
	v_mfma_f32_16x16x32_f16 v[70:73], v[122:125], v[146:149], v[70:73]
	v_mfma_f32_16x16x32_f16 v[46:49], v[122:125], v[150:153], v[46:49]
	v_mfma_f32_16x16x32_f16 v[240:243], v[122:125], v[154:157], v[240:243]
	v_mfma_f32_16x16x32_f16 v[66:69], v[126:129], v[146:149], v[66:69]
	v_mfma_f32_16x16x32_f16 v[42:45], v[126:129], v[150:153], v[42:45]
	v_mfma_f32_16x16x32_f16 v[236:239], v[126:129], v[154:157], v[236:239]
	v_mfma_f32_16x16x32_f16 v[62:65], v[130:133], v[146:149], v[62:65]
	v_mfma_f32_16x16x32_f16 v[38:41], v[130:133], v[150:153], v[38:41]
	v_mfma_f32_16x16x32_f16 v[34:37], v[130:133], v[154:157], v[34:37]
	s_waitcnt lgkmcnt(0)
	ds_read_b128 v[146:149], v165
	v_mfma_f32_16x16x32_f16 v[82:85], v[86:89], v[134:137], v[82:85]
	ds_read_b128 v[150:153], v165 offset:2048
	v_mfma_f32_16x16x32_f16 v[58:61], v[86:89], v[138:141], v[58:61]
	ds_read_b128 v[154:157], v165 offset:4096
	v_mfma_f32_16x16x32_f16 v[14:17], v[86:89], v[142:145], v[14:17]
	ds_read_b128 v[110:113], v161
	v_mfma_f32_16x16x32_f16 v[78:81], v[90:93], v[134:137], v[78:81]
	ds_read_b128 v[114:117], v161 offset:2048
	v_mfma_f32_16x16x32_f16 v[22:25], v[90:93], v[138:141], v[22:25]
	ds_read_b128 v[118:121], v161 offset:4096
	v_mfma_f32_16x16x32_f16 v[30:33], v[90:93], v[142:145], v[30:33]
	ds_read_b128 v[122:125], v161 offset:6144
	v_mfma_f32_16x16x32_f16 v[74:77], v[94:97], v[134:137], v[74:77]
	ds_read_b128 v[126:129], v161 offset:8192
	v_mfma_f32_16x16x32_f16 v[18:21], v[94:97], v[138:141], v[18:21]
	ds_read_b128 v[130:133], v161 offset:10240
	v_mfma_f32_16x16x32_f16 v[26:29], v[94:97], v[142:145], v[26:29]
	v_mfma_f32_16x16x32_f16 v[70:73], v[98:101], v[134:137], v[70:73]
	v_mfma_f32_16x16x32_f16 v[46:49], v[98:101], v[138:141], v[46:49]
	v_mfma_f32_16x16x32_f16 v[240:243], v[98:101], v[142:145], v[240:243]
	v_mfma_f32_16x16x32_f16 v[66:69], v[102:105], v[134:137], v[66:69]
	v_mfma_f32_16x16x32_f16 v[42:45], v[102:105], v[138:141], v[42:45]
	v_mfma_f32_16x16x32_f16 v[236:239], v[102:105], v[142:145], v[236:239]
	v_mfma_f32_16x16x32_f16 v[62:65], v[106:109], v[134:137], v[62:65]
	v_mfma_f32_16x16x32_f16 v[38:41], v[106:109], v[138:141], v[38:41]
	v_mfma_f32_16x16x32_f16 v[34:37], v[106:109], v[142:145], v[34:37]
	s_waitcnt vmcnt(3) lgkmcnt(0)
	s_barrier
	ds_read_b128 v[134:137], v162
	v_mfma_f32_16x16x32_f16 v[82:85], v[110:113], v[146:149], v[82:85]
	ds_read_b128 v[138:141], v162 offset:2048
	v_mfma_f32_16x16x32_f16 v[58:61], v[110:113], v[150:153], v[58:61]
	ds_read_b128 v[142:145], v162 offset:4096
	v_mfma_f32_16x16x32_f16 v[14:17], v[110:113], v[154:157], v[14:17]
	ds_read_b128 v[86:89], v158
	v_mfma_f32_16x16x32_f16 v[78:81], v[114:117], v[146:149], v[78:81]
	ds_read_b128 v[90:93], v158 offset:2048
	v_mfma_f32_16x16x32_f16 v[22:25], v[114:117], v[150:153], v[22:25]
	ds_read_b128 v[94:97], v158 offset:4096
	v_mfma_f32_16x16x32_f16 v[30:33], v[114:117], v[154:157], v[30:33]
	ds_read_b128 v[98:101], v158 offset:6144
	v_mfma_f32_16x16x32_f16 v[74:77], v[118:121], v[146:149], v[74:77]
	ds_read_b128 v[102:105], v158 offset:8192
	v_mfma_f32_16x16x32_f16 v[18:21], v[118:121], v[150:153], v[18:21]
	ds_read_b128 v[106:109], v158 offset:10240
	v_mfma_f32_16x16x32_f16 v[26:29], v[118:121], v[154:157], v[26:29]
	v_mfma_f32_16x16x32_f16 v[70:73], v[122:125], v[146:149], v[70:73]
	v_mfma_f32_16x16x32_f16 v[46:49], v[122:125], v[150:153], v[46:49]
	v_mfma_f32_16x16x32_f16 v[240:243], v[122:125], v[154:157], v[240:243]
	v_mfma_f32_16x16x32_f16 v[66:69], v[126:129], v[146:149], v[66:69]
	v_mfma_f32_16x16x32_f16 v[42:45], v[126:129], v[150:153], v[42:45]
	v_mfma_f32_16x16x32_f16 v[236:239], v[126:129], v[154:157], v[236:239]
	v_mfma_f32_16x16x32_f16 v[62:65], v[130:133], v[146:149], v[62:65]
	v_mfma_f32_16x16x32_f16 v[38:41], v[130:133], v[150:153], v[38:41]
	v_mfma_f32_16x16x32_f16 v[34:37], v[130:133], v[154:157], v[34:37]
	s_waitcnt lgkmcnt(0)
	ds_read_b128 v[146:149], v164
	v_mfma_f32_16x16x32_f16 v[82:85], v[86:89], v[134:137], v[82:85]
	ds_read_b128 v[150:153], v164 offset:2048
	v_mfma_f32_16x16x32_f16 v[58:61], v[86:89], v[138:141], v[58:61]
	ds_read_b128 v[154:157], v164 offset:4096
	v_mfma_f32_16x16x32_f16 v[14:17], v[86:89], v[142:145], v[14:17]
	ds_read_b128 v[110:113], v160
	v_mfma_f32_16x16x32_f16 v[78:81], v[90:93], v[134:137], v[78:81]
	ds_read_b128 v[114:117], v160 offset:2048
	v_mfma_f32_16x16x32_f16 v[22:25], v[90:93], v[138:141], v[22:25]
	ds_read_b128 v[118:121], v160 offset:4096
	v_mfma_f32_16x16x32_f16 v[30:33], v[90:93], v[142:145], v[30:33]
	ds_read_b128 v[122:125], v160 offset:6144
	v_mfma_f32_16x16x32_f16 v[74:77], v[94:97], v[134:137], v[74:77]
	ds_read_b128 v[126:129], v160 offset:8192
	v_mfma_f32_16x16x32_f16 v[18:21], v[94:97], v[138:141], v[18:21]
	ds_read_b128 v[130:133], v160 offset:10240
	v_mfma_f32_16x16x32_f16 v[26:29], v[94:97], v[142:145], v[26:29]
	v_mfma_f32_16x16x32_f16 v[70:73], v[98:101], v[134:137], v[70:73]
	v_mfma_f32_16x16x32_f16 v[46:49], v[98:101], v[138:141], v[46:49]
	v_mfma_f32_16x16x32_f16 v[240:243], v[98:101], v[142:145], v[240:243]
	v_mfma_f32_16x16x32_f16 v[66:69], v[102:105], v[134:137], v[66:69]
	v_mfma_f32_16x16x32_f16 v[42:45], v[102:105], v[138:141], v[42:45]
	v_mfma_f32_16x16x32_f16 v[236:239], v[102:105], v[142:145], v[236:239]
	v_mfma_f32_16x16x32_f16 v[62:65], v[106:109], v[134:137], v[62:65]
	v_mfma_f32_16x16x32_f16 v[38:41], v[106:109], v[138:141], v[38:41]
	v_mfma_f32_16x16x32_f16 v[34:37], v[106:109], v[142:145], v[34:37]
	s_waitcnt lgkmcnt(0)
	v_mfma_f32_16x16x32_f16 v[82:85], v[110:113], v[146:149], v[82:85]
	v_mfma_f32_16x16x32_f16 v[58:61], v[110:113], v[150:153], v[58:61]
	v_mfma_f32_16x16x32_f16 v[14:17], v[110:113], v[154:157], v[14:17]
	v_mfma_f32_16x16x32_f16 v[78:81], v[114:117], v[146:149], v[78:81]
	v_mfma_f32_16x16x32_f16 v[22:25], v[114:117], v[150:153], v[22:25]
	v_mfma_f32_16x16x32_f16 v[30:33], v[114:117], v[154:157], v[30:33]
	v_mfma_f32_16x16x32_f16 v[74:77], v[118:121], v[146:149], v[74:77]
	v_mfma_f32_16x16x32_f16 v[18:21], v[118:121], v[150:153], v[18:21]
	v_mfma_f32_16x16x32_f16 v[26:29], v[118:121], v[154:157], v[26:29]
	v_mfma_f32_16x16x32_f16 v[70:73], v[122:125], v[146:149], v[70:73]
	v_mfma_f32_16x16x32_f16 v[46:49], v[122:125], v[150:153], v[46:49]
	v_mfma_f32_16x16x32_f16 v[240:243], v[122:125], v[154:157], v[240:243]
	v_mfma_f32_16x16x32_f16 v[66:69], v[126:129], v[146:149], v[66:69]
	v_mfma_f32_16x16x32_f16 v[42:45], v[126:129], v[150:153], v[42:45]
	v_mfma_f32_16x16x32_f16 v[236:239], v[126:129], v[154:157], v[236:239]
	v_mfma_f32_16x16x32_f16 v[62:65], v[130:133], v[146:149], v[62:65]
	v_mfma_f32_16x16x32_f16 v[38:41], v[130:133], v[150:153], v[38:41]
	v_mfma_f32_16x16x32_f16 v[34:37], v[130:133], v[154:157], v[34:37]
